# union3 + prologue prep_rows loop rescheduled like the resid loops (next-row loads overlap the row arithmetic)
# speedup vs baseline: 1.0016x; 1.0016x over previous
; #define GAS __attribute__((address_space(1)))
; __device__ __forceinline__ void prep_rows(const float* Xin, bf16* Xo, unsigned char* XQv, float* RSv, float* RQv, int m0, int mstep, int lane) {
;     ...
;     while (m < M) { const int mn = m + mstep;
;         if (mn < M) { const GAS f32x4* xr = (const GAS f32x4*)(Xin + (size_t)mn * DM) + lane;
; #pragma unroll
;             for (int j = 0; j < 8; ++j) n[j] = __builtin_nontemporal_load(xr + 64 * j); }
;     ...
;         for (int j = 0; j < 8; ++j) v[j] = n[j];
;         m = mn; }
.LBB0_71:
	s_or_b64 exec, exec, s[20:21]
	s_add_u32 s8, s8, s10
	s_addc_u32 s9, s9, s11
	v_lshl_add_u64 v[66:67], v[66:67], 0, s[12:13]
	v_lshl_add_u64 v[68:69], v[68:69], 0, s[14:15]
	v_lshl_add_u64 v[70:71], v[70:71], 0, s[16:17]
	s_and_b64 vcc, exec, s[18:19]
	v_mov_b32_e32 v62, v30
	v_mov_b32_e32 v63, v31
	v_mov_b32_e32 v64, v32
	v_mov_b32_e32 v65, v33
	v_mov_b32_e32 v58, v26
	v_mov_b32_e32 v59, v27
	v_mov_b32_e32 v60, v28
	v_mov_b32_e32 v61, v29
	v_mov_b32_e32 v54, v22
	v_mov_b32_e32 v55, v23
	v_mov_b32_e32 v56, v24
	v_mov_b32_e32 v57, v25
	v_mov_b32_e32 v50, v18
	v_mov_b32_e32 v51, v19
	v_mov_b32_e32 v52, v20
	v_mov_b32_e32 v53, v21
	v_mov_b32_e32 v46, v14
	v_mov_b32_e32 v47, v15
	v_mov_b32_e32 v48, v16
	v_mov_b32_e32 v49, v17
	v_mov_b32_e32 v42, v10
	v_mov_b32_e32 v43, v11
	v_mov_b32_e32 v44, v12
	v_mov_b32_e32 v45, v13
	v_mov_b32_e32 v38, v6
	v_mov_b32_e32 v39, v7
	v_mov_b32_e32 v40, v8
	v_mov_b32_e32 v41, v9
	v_mov_b32_e32 v34, v2
	v_mov_b32_e32 v35, v3
	v_mov_b32_e32 v36, v4
	v_mov_b32_e32 v37, v5
	s_cbranch_vccnz .LBB0_76
	s_add_i32 s28, s28, s94
	s_cmpk_gt_i32 s28, 0x3fff
	s_cselect_b64 s[18:19], -1, 0
	s_and_b64 vcc, exec, s[18:19]
	s_cbranch_vccnz .LBB0_74
	global_load_dwordx4 v[30:33], v[70:71], off offset:-4096 nt
	global_load_dwordx4 v[26:29], v[70:71], off offset:-3072 nt
	global_load_dwordx4 v[22:25], v[70:71], off offset:-2048 nt
	global_load_dwordx4 v[18:21], v[70:71], off offset:-1024 nt
	global_load_dwordx4 v[14:17], v[70:71], off nt
	global_load_dwordx4 v[10:13], v[70:71], off offset:1024 nt
	global_load_dwordx4 v[6:9], v[70:71], off offset:2048 nt
	global_load_dwordx4 v[2:5], v[70:71], off offset:3072 nt
	s_branch .LBB0_74
.LBB0_72:
	s_add_i32 s28, s28, s94
	s_cmpk_gt_i32 s28, 0x3fff
	s_cselect_b64 s[18:19], -1, 0
	s_and_b64 vcc, exec, s[18:19]
	s_cbranch_vccnz .Lprep_nonext
	global_load_dwordx4 v[30:33], v[70:71], off offset:-4096 nt
	global_load_dwordx4 v[26:29], v[70:71], off offset:-3072 nt
	global_load_dwordx4 v[22:25], v[70:71], off offset:-2048 nt
	global_load_dwordx4 v[18:21], v[70:71], off offset:-1024 nt
	global_load_dwordx4 v[14:17], v[70:71], off nt
	global_load_dwordx4 v[10:13], v[70:71], off offset:1024 nt
	global_load_dwordx4 v[6:9], v[70:71], off offset:2048 nt
	global_load_dwordx4 v[2:5], v[70:71], off offset:3072 nt
	s_waitcnt vmcnt(8)
	s_branch .LBB0_74

; #define GAS __attribute__((address_space(1)))
; __device__ __forceinline__ unsigned pk2(float lo, float hi) { f32x2_t_ v = {lo, hi}; bf16x2_t_ b = __builtin_convertvector(v, bf16x2_t_); return __builtin_bit_cast(unsigned, b); }
; __device__ __forceinline__ float quant_row(const f32x4 (&v)[8], unsigned char* xq, int lane) {
;     ...
;     for (int j = 0; j < 8; ++j) mx = __builtin_fmaxf(mx, __builtin_fmaxf(__builtin_fmaxf(__builtin_fabsf(v[j].x), __builtin_fabsf(v[j].y)), __builtin_fmaxf(__builtin_fabsf(v[j].z), __builtin_fabsf(v[j].w))));
;     mx = __builtin_fmaxf(wave_max(mx), 1e-20f);
; __device__ __forceinline__ void prep_rows(const float* Xin, bf16* Xo, unsigned char* XQv, float* RSv, float* RQv, int m0, int mstep, int lane) {
;     ...
;         float s = 0.f;
; #pragma unroll
;         for (int j = 0; j < 8; ++j) s += (v[j].x * v[j].x + v[j].y * v[j].y) + (v[j].z * v[j].z + v[j].w * v[j].w);
;         s = wave_sum(s);
;         GAS v2u* o8 = (GAS v2u*)(Xo + (size_t)m * DM) + lane;
; #pragma unroll
;         for (int j = 0; j < 8; ++j) { v2u w; w.x = pk2(v[j].x, v[j].y); w.y = pk2(v[j].z, v[j].w); o8[64 * j] = w; }
.LBB0_74:
	v_mul_f32_e32 v80, v63, v63
	v_mul_f32_e32 v81, v65, v65
	v_fmac_f32_e32 v80, v62, v62
	v_fmac_f32_e32 v81, v64, v64
	v_add_f32_e32 v80, v80, v81
	v_mul_f32_e32 v81, v59, v59
	v_mul_f32_e32 v82, v61, v61
	v_fmac_f32_e32 v81, v58, v58
	v_fmac_f32_e32 v82, v60, v60
	v_add_f32_e32 v81, v81, v82
	v_add_f32_e32 v80, v80, v81
	v_mul_f32_e32 v81, v55, v55
	v_mul_f32_e32 v82, v57, v57
	v_fmac_f32_e32 v81, v54, v54
	v_fmac_f32_e32 v82, v56, v56
	v_add_f32_e32 v81, v81, v82
	v_add_f32_e32 v80, v81, v80
	v_mul_f32_e32 v81, v51, v51
	v_mul_f32_e32 v82, v53, v53
	v_fmac_f32_e32 v81, v50, v50
	v_fmac_f32_e32 v82, v52, v52
	v_add_f32_e32 v81, v81, v82
	v_add_f32_e32 v80, v81, v80
	v_mul_f32_e32 v81, v47, v47
	v_mul_f32_e32 v82, v49, v49
	v_fmac_f32_e32 v81, v46, v46
	v_fmac_f32_e32 v82, v48, v48
	v_add_f32_e32 v81, v81, v82
	v_add_f32_e32 v80, v81, v80
	v_mul_f32_e32 v81, v43, v43
	v_mul_f32_e32 v82, v45, v45
	v_fmac_f32_e32 v81, v42, v42
	v_fmac_f32_e32 v82, v44, v44
	v_add_f32_e32 v81, v81, v82
	v_add_f32_e32 v80, v81, v80
	v_mul_f32_e32 v81, v39, v39
	v_mul_f32_e32 v82, v41, v41
	v_fmac_f32_e32 v81, v38, v38
	v_fmac_f32_e32 v82, v40, v40
	v_add_f32_e32 v81, v81, v82
	v_add_f32_e32 v80, v81, v80
	v_mul_f32_e32 v81, v35, v35
	v_mul_f32_e32 v82, v37, v37
	v_fmac_f32_e32 v81, v34, v34
	v_fmac_f32_e32 v82, v36, v36
	v_add_f32_e32 v81, v81, v82
	v_add_f32_e32 v80, v81, v80
	ds_bpermute_b32 v81, v0, v80
	v_max_f32_e64 v82, |v64|, |v64|
	v_max_f32_e64 v83, |v60|, |v60|
	v_max_f32_e64 v84, |v52|, |v52|
	v_cvt_pk_bf16_f32 v85, v64, v65
	s_waitcnt lgkmcnt(0)
	v_add_f32_e32 v80, v80, v81
	ds_bpermute_b32 v81, v1, v80
	s_waitcnt lgkmcnt(0)
	v_add_f32_e32 v80, v80, v81
	ds_bpermute_b32 v81, v72, v80
	s_waitcnt lgkmcnt(0)
	v_add_f32_e32 v80, v80, v81
	ds_bpermute_b32 v81, v73, v80
	s_waitcnt lgkmcnt(0)
	v_add_f32_e32 v80, v80, v81
	ds_bpermute_b32 v81, v74, v80
	s_waitcnt lgkmcnt(0)
	v_add_f32_e32 v80, v80, v81
	v_max_f32_e64 v81, |v65|, |v65|
	v_max_f32_e32 v81, v82, v81
	v_max_f32_e64 v82, |v61|, |v61|
	v_max_f32_e32 v82, v83, v82
	v_max3_f32 v81, |v62|, |v63|, v81
	v_max3_f32 v82, |v58|, |v59|, v82
	v_max3_f32 v81, v81, 0, v82
	v_max_f32_e64 v82, |v57|, |v57|
	v_max_f32_e64 v83, |v56|, |v56|
	v_max_f32_e32 v82, v83, v82
	v_max_f32_e64 v83, |v53|, |v53|
	v_max_f32_e32 v83, v84, v83
	v_max3_f32 v82, |v54|, |v55|, v82
	v_max3_f32 v83, |v50|, |v51|, v83
	v_max3_f32 v81, v81, v82, v83
	v_max_f32_e64 v82, |v49|, |v49|
	v_max_f32_e64 v83, |v48|, |v48|
	v_max_f32_e32 v82, v83, v82
	v_max_f32_e64 v83, |v45|, |v45|
	v_max_f32_e64 v84, |v44|, |v44|
	v_max_f32_e32 v83, v84, v83
	v_max3_f32 v82, |v46|, |v47|, v82
	v_max3_f32 v83, |v42|, |v43|, v83
	v_max3_f32 v81, v81, v82, v83
	v_max_f32_e64 v82, |v41|, |v41|
	v_max_f32_e64 v83, |v40|, |v40|
	v_max_f32_e32 v82, v83, v82
	v_max_f32_e64 v83, |v37|, |v37|
	v_max_f32_e64 v84, |v36|, |v36|
	v_max_f32_e32 v83, v84, v83
	v_max3_f32 v82, |v38|, |v39|, v82
	v_max3_f32 v83, |v34|, |v35|, v83
	v_max3_f32 v86, v81, v82, v83
	ds_bpermute_b32 v87, v0, v86
	v_lshl_add_u64 v[82:83], s[84:85], 0, v[68:69]
	v_cvt_pk_bf16_f32 v84, v62, v63
	ds_bpermute_b32 v81, v75, v80
	s_waitcnt lgkmcnt(1)
	v_max_f32_e32 v87, v87, v87
	v_max_f32_e32 v88, v86, v87
	ds_bpermute_b32 v89, v1, v88
	v_add_co_u32_e32 v86, vcc, s22, v82
	v_cvt_pk_bf16_f32 v82, v58, v59
	s_nop 0
	v_addc_co_u32_e32 v87, vcc, 0, v83, vcc
	s_waitcnt vmcnt(0)
	global_store_dwordx2 v[86:87], v[84:85], off
	s_waitcnt lgkmcnt(0)
	v_max_f32_e32 v84, v89, v89
	v_max_f32_e32 v84, v88, v84
	ds_bpermute_b32 v85, v72, v84
	v_cvt_pk_bf16_f32 v83, v60, v61
	global_store_dwordx2 v[86:87], v[82:83], off offset:512
	v_cvt_pk_bf16_f32 v82, v54, v55
	v_cvt_pk_bf16_f32 v83, v56, v57
	global_store_dwordx2 v[86:87], v[82:83], off offset:1024
	s_waitcnt lgkmcnt(0)
	v_max_f32_e32 v82, v85, v85
	v_max_f32_e32 v84, v84, v82
	ds_bpermute_b32 v85, v73, v84
	v_cvt_pk_bf16_f32 v82, v50, v51
	v_cvt_pk_bf16_f32 v83, v52, v53
	global_store_dwordx2 v[86:87], v[82:83], off offset:1536
	v_cvt_pk_bf16_f32 v82, v46, v47
	s_waitcnt lgkmcnt(0)
	v_max_f32_e32 v83, v85, v85
	v_max_f32_e32 v84, v84, v83
	ds_bpermute_b32 v85, v74, v84
	v_cvt_pk_bf16_f32 v83, v48, v49
	global_store_dwordx2 v[86:87], v[82:83], off offset:2048
	v_cvt_pk_bf16_f32 v82, v42, v43
	v_cvt_pk_bf16_f32 v83, v44, v45
	s_waitcnt lgkmcnt(0)
	v_max_f32_e32 v85, v85, v85
	v_max_f32_e32 v84, v84, v85
	ds_bpermute_b32 v85, v75, v84
	global_store_dwordx2 v[86:87], v[82:83], off offset:2560
	v_cvt_pk_bf16_f32 v82, v38, v39
	v_cvt_pk_bf16_f32 v83, v40, v41
	global_store_dwordx2 v[86:87], v[82:83], off offset:3072
	s_waitcnt lgkmcnt(0)
; #define GAS __attribute__((address_space(1)))
; __device__ __forceinline__ float quant_row(const f32x4 (&v)[8], unsigned char* xq, int lane) {
;     ...
;     mx = __builtin_fmaxf(wave_max(mx), 1e-20f);
;     const float q = 127.0f / mx;
;     GAS unsigned* o4 = (GAS unsigned*)xq + lane;
; #pragma unroll
;     for (int j = 0; j < 8; ++j) o4[64 * j] = q4(v[j], q);
;     return mx * (1.0f / 127.0f);
; __device__ __forceinline__ void prep_rows(const float* Xin, bf16* Xo, unsigned char* XQv, float* RSv, float* RQv, int m0, int mstep, int lane) {
;     ...
;         const float dq = quant_row(v, XQv + (size_t)m * DM, lane);
;         if (lane == 0) { const float r = 1.f / sqrtf(s * (1.f / DM) + NORM_EPS); RSv[m] = r; RQv[m] = r * dq; }
	v_max3_f32 v82, v84, v85, s23
	v_div_scale_f32 v83, s[6:7], v82, v82, s24
	v_rcp_f32_e32 v88, v83
	v_cvt_pk_bf16_f32 v84, v34, v35
	v_cvt_pk_bf16_f32 v85, v36, v37
	global_store_dwordx2 v[86:87], v[84:85], off offset:3584
	v_fma_f32 v84, -v83, v88, 1.0
	v_fmac_f32_e32 v88, v84, v88
	v_div_scale_f32 v84, vcc, s24, v82, s24
	v_mul_f32_e32 v85, v84, v88
	v_fma_f32 v86, -v83, v85, v84
	v_fmac_f32_e32 v85, v86, v88
	v_fma_f32 v83, -v83, v85, v84
	v_div_fmas_f32 v83, v83, v88, v85
	v_div_fixup_f32 v83, v83, v82, s24
	v_mul_f32_e32 v63, v63, v83
	v_mul_f32_e32 v62, v62, v83
	v_rndne_f32_e32 v63, v63
	v_mul_f32_e32 v64, v64, v83
	v_mul_f32_e32 v65, v65, v83
	v_mul_f32_e32 v59, v59, v83
	v_mul_f32_e32 v55, v55, v83
	v_mul_f32_e32 v51, v51, v83
	v_mul_f32_e32 v47, v47, v83
	v_mul_f32_e32 v43, v43, v83
	v_mul_f32_e32 v39, v39, v83
	v_mul_f32_e32 v35, v35, v83
	v_rndne_f32_e32 v62, v62
	v_cvt_i32_f32_e32 v63, v63
	v_rndne_f32_e32 v64, v64
	v_rndne_f32_e32 v65, v65
	v_mul_f32_e32 v58, v58, v83
	v_rndne_f32_e32 v59, v59
	v_mul_f32_e32 v60, v60, v83
	v_mul_f32_e32 v61, v61, v83
	v_mul_f32_e32 v54, v54, v83
	v_rndne_f32_e32 v55, v55
	v_mul_f32_e32 v56, v56, v83
	v_mul_f32_e32 v57, v57, v83
	v_mul_f32_e32 v50, v50, v83
	v_rndne_f32_e32 v51, v51
	v_mul_f32_e32 v52, v52, v83
	v_mul_f32_e32 v53, v53, v83
	v_mul_f32_e32 v46, v46, v83
	v_rndne_f32_e32 v47, v47
	v_mul_f32_e32 v48, v48, v83
	v_mul_f32_e32 v49, v49, v83
	v_mul_f32_e32 v42, v42, v83
	v_rndne_f32_e32 v43, v43
	v_mul_f32_e32 v44, v44, v83
	v_mul_f32_e32 v45, v45, v83
	v_mul_f32_e32 v38, v38, v83
	v_rndne_f32_e32 v39, v39
	v_mul_f32_e32 v40, v40, v83
	v_mul_f32_e32 v41, v41, v83
	v_mul_f32_e32 v34, v34, v83
	v_rndne_f32_e32 v35, v35
	v_mul_f32_e32 v36, v36, v83
	v_mul_f32_e32 v37, v37, v83
	v_cvt_i32_f32_e32 v62, v62
	v_cvt_i32_f32_sdwa v64, v64 dst_sel:WORD_1 dst_unused:UNUSED_PAD src0_sel:DWORD
	v_cvt_i32_f32_e32 v65, v65
	v_rndne_f32_e32 v58, v58
	v_cvt_i32_f32_e32 v59, v59
	v_rndne_f32_e32 v60, v60
	v_rndne_f32_e32 v61, v61
	v_rndne_f32_e32 v54, v54
	v_cvt_i32_f32_e32 v55, v55
	v_rndne_f32_e32 v56, v56
	v_rndne_f32_e32 v57, v57
	v_rndne_f32_e32 v50, v50
	v_cvt_i32_f32_e32 v51, v51
	v_rndne_f32_e32 v52, v52
	v_rndne_f32_e32 v53, v53
	v_rndne_f32_e32 v46, v46
	v_cvt_i32_f32_e32 v47, v47
	v_rndne_f32_e32 v48, v48
	v_rndne_f32_e32 v49, v49
	v_rndne_f32_e32 v42, v42
	v_cvt_i32_f32_e32 v43, v43
	v_rndne_f32_e32 v44, v44
	v_rndne_f32_e32 v45, v45
	v_rndne_f32_e32 v38, v38
	v_cvt_i32_f32_e32 v39, v39
	v_rndne_f32_e32 v40, v40
	v_rndne_f32_e32 v41, v41
	v_rndne_f32_e32 v34, v34
	v_cvt_i32_f32_e32 v35, v35
	v_rndne_f32_e32 v36, v36
	v_rndne_f32_e32 v37, v37
	v_cvt_i32_f32_e32 v58, v58
	v_cvt_i32_f32_sdwa v60, v60 dst_sel:WORD_1 dst_unused:UNUSED_PAD src0_sel:DWORD
	v_cvt_i32_f32_e32 v61, v61
	v_cvt_i32_f32_e32 v54, v54
	v_cvt_i32_f32_sdwa v56, v56 dst_sel:WORD_1 dst_unused:UNUSED_PAD src0_sel:DWORD
	v_cvt_i32_f32_e32 v57, v57
	v_cvt_i32_f32_e32 v50, v50
	v_cvt_i32_f32_sdwa v52, v52 dst_sel:WORD_1 dst_unused:UNUSED_PAD src0_sel:DWORD
	v_cvt_i32_f32_e32 v53, v53
	v_cvt_i32_f32_e32 v46, v46
	v_cvt_i32_f32_sdwa v48, v48 dst_sel:WORD_1 dst_unused:UNUSED_PAD src0_sel:DWORD
	v_cvt_i32_f32_e32 v49, v49
	v_cvt_i32_f32_e32 v42, v42
	v_cvt_i32_f32_sdwa v44, v44 dst_sel:WORD_1 dst_unused:UNUSED_PAD src0_sel:DWORD
	v_cvt_i32_f32_e32 v45, v45
	v_cvt_i32_f32_e32 v38, v38
	v_cvt_i32_f32_sdwa v40, v40 dst_sel:WORD_1 dst_unused:UNUSED_PAD src0_sel:DWORD
	v_cvt_i32_f32_e32 v41, v41
	v_cvt_i32_f32_e32 v34, v34
	v_cvt_i32_f32_sdwa v36, v36 dst_sel:WORD_1 dst_unused:UNUSED_PAD src0_sel:DWORD
	v_cvt_i32_f32_e32 v37, v37
	v_lshlrev_b32_e32 v63, 8, v63
	v_lshl_add_u64 v[84:85], s[84:85], 0, v[66:67]
	v_and_b32_e32 v63, 0xff00, v63
	v_and_b32_e32 v64, 0xff0000, v64
	v_perm_b32 v62, v65, v62, s25
	v_lshlrev_b32_e32 v59, 8, v59
	v_lshlrev_b32_e32 v55, 8, v55
	v_lshlrev_b32_e32 v51, 8, v51
	v_lshlrev_b32_e32 v47, 8, v47
	v_lshlrev_b32_e32 v43, 8, v43
	v_lshlrev_b32_e32 v39, 8, v39
	v_lshlrev_b32_e32 v35, 8, v35
	v_or3_b32 v64, v62, v63, v64
	v_add_co_u32_e32 v62, vcc, s26, v84
	v_and_b32_e32 v59, 0xff00, v59
	v_and_b32_e32 v60, 0xff0000, v60
	v_perm_b32 v58, v61, v58, s25
	v_and_b32_e32 v55, 0xff00, v55
	v_and_b32_e32 v56, 0xff0000, v56
	v_perm_b32 v54, v57, v54, s25
	v_and_b32_e32 v51, 0xff00, v51
	v_and_b32_e32 v52, 0xff0000, v52
	v_perm_b32 v50, v53, v50, s25
	v_and_b32_e32 v47, 0xff00, v47
	v_and_b32_e32 v48, 0xff0000, v48
	v_perm_b32 v46, v49, v46, s25
	v_and_b32_e32 v43, 0xff00, v43
	v_and_b32_e32 v44, 0xff0000, v44
	v_perm_b32 v42, v45, v42, s25
	v_and_b32_e32 v39, 0xff00, v39
	v_and_b32_e32 v40, 0xff0000, v40
	v_perm_b32 v38, v41, v38, s25
	v_and_b32_e32 v35, 0xff00, v35
	v_and_b32_e32 v36, 0xff0000, v36
	v_perm_b32 v34, v37, v34, s25
	v_addc_co_u32_e32 v63, vcc, 0, v85, vcc
	v_or3_b32 v58, v58, v59, v60
	v_or3_b32 v54, v54, v55, v56
	v_or3_b32 v50, v50, v51, v52
	v_or3_b32 v46, v46, v47, v48
	v_or3_b32 v42, v42, v43, v44
	v_or3_b32 v38, v38, v39, v40
	v_or3_b32 v34, v34, v35, v36
	global_store_dword v[62:63], v64, off
	global_store_dword v[62:63], v58, off offset:256
	global_store_dword v[62:63], v54, off offset:512
	global_store_dword v[62:63], v50, off offset:768
	global_store_dword v[62:63], v46, off offset:1024
	global_store_dword v[62:63], v42, off offset:1280
	global_store_dword v[62:63], v38, off offset:1536
	global_store_dword v[62:63], v34, off offset:1792
	s_and_saveexec_b64 s[20:21], s[4:5]
	s_cbranch_execz .LBB0_71
	v_add_f32_e32 v34, v80, v81
	v_fmamk_f32 v34, v34, 0x3a000000, v76
	v_mul_f32_e32 v35, 0x4f800000, v34
	v_cmp_gt_f32_e32 vcc, s27, v34
	s_nop 1
	v_cndmask_b32_e32 v34, v34, v35, vcc
	v_sqrt_f32_e32 v35, v34
	s_nop 0
	v_add_u32_e32 v36, -1, v35
	v_fma_f32 v38, -v36, v35, v34
	v_add_u32_e32 v37, 1, v35
	v_cmp_ge_f32_e64 s[6:7], 0, v38
	s_nop 1
	v_cndmask_b32_e64 v36, v35, v36, s[6:7]
	v_fma_f32 v35, -v37, v35, v34
	v_cmp_lt_f32_e64 s[6:7], 0, v35
	s_nop 1
	v_cndmask_b32_e64 v35, v36, v37, s[6:7]
	v_mul_f32_e32 v36, 0x37800000, v35
	v_cndmask_b32_e32 v35, v35, v36, vcc
	v_cmp_class_f32_e32 vcc, v34, v77
	v_mul_f32_e32 v37, 0x3c010204, v82
	s_nop 0
	v_cndmask_b32_e32 v34, v35, v34, vcc
	v_div_scale_f32 v35, s[6:7], v34, v34, 1.0
	v_rcp_f32_e32 v36, v35
	s_add_u32 s6, s84, s8
	s_addc_u32 s7, s85, s9
	v_fma_f32 v38, -v35, v36, 1.0
	v_fmac_f32_e32 v36, v38, v36
	v_div_scale_f32 v38, vcc, 1.0, v34, 1.0
	v_mul_f32_e32 v39, v38, v36
	v_fma_f32 v40, -v35, v39, v38
	v_fmac_f32_e32 v39, v40, v36
	v_fma_f32 v35, -v35, v39, v38
	v_div_fmas_f32 v35, v35, v36, v39
	v_div_fixup_f32 v34, v35, v34, 1.0
	global_store_dword v78, v34, s[6:7]
	v_mul_f32_e32 v34, v34, v37
	global_store_dword v79, v34, s[6:7]
	s_branch .LBB0_71
